# final phase: streaming (nt) hint on the f32 output stores and on the last-use H / routed-row loads
# speedup vs baseline: 1.0071x; 1.0011x over previous
; DI unsigned pk2(float lo, float hi) { return cvt_pk_bf16(lo, hi); }
; #define CMB_FENCE() do { asm volatile("" ::: "memory"); __builtin_amdgcn_sched_barrier(0); } while (0)
; #define CMB_LOADH(HP, row_) do { _Pragma("unroll") for (int j = 0; j < 8; ++j) HP[j] = *(const u32x2*)(H + (size_t)(row_) * DM + 4 * lane + 256 * j); } while (0)
; template <bool LAST> DI void cmb_block(bf16_t* H, const bf16_t* Y, const int* inv, const float* g2, const float* gain1, const float* shift, const float* scale, bf16_t* A, float* out, int row0, int n, int lane) {
;     u32x2 gvp[8], Gmp[8], shp[8];
;     { f32x4 t0[8], t1[8], t2[8], t3[8];
; #pragma unroll
;       for (int j = 0; j < 8; ++j) { const int c = 4 * lane + 256 * j; t0[j] = *(const f32x4*)(g2 + c); if (!LAST) { t1[j] = *(const f32x4*)(gain1 + c); t2[j] = *(const f32x4*)(scale + c); t3[j] = *(const f32x4*)(shift + c); } }
;       CMB_FENCE();
; #pragma unroll
;       for (int j = 0; j < 8; ++j) { const f32x4 t = t0[j] * Y8_INV; gvp[j].x = pk2(t[0], t[1]); gvp[j].y = pk2(t[2], t[3]);
;         if (!LAST) { const f32x4 gm = t1[j] * (t2[j] + 1.0f); Gmp[j].x = pk2(gm[0], gm[1]); Gmp[j].y = pk2(gm[2], gm[3]); shp[j].x = pk2(t3[j][0], t3[j][1]); shp[j].y = pk2(t3[j][2], t3[j][3]); } }
;       CMB_FENCE(); }
;     ...
;     u32x2 hp[8], hn[8]; int iv0, iv1 = -1, iv2 = -1;
;     unsigned q1[8], q2[8]; unsigned m; float f1, f2;
;     ...
;     CMB_LOADH(hp, row0); iv0 = CMB_INV(row0); if (n > 1) iv1 = CMB_INV(row0 + 1);
;     m = (unsigned)(__ballot(iv0 >= 0) & 0xFFFFull);
;     CMB_GATHER(iv0);
.LBB0_2030:
	s_ashr_i32 s7, s12, 8
	s_lshl_b32 s6, s12, 3
	s_mul_hi_i32 s9, s7, 0xc000
	s_mul_i32 s7, s7, 0xc000
	s_add_u32 s8, s82, s7
	s_addc_u32 s9, s83, s9
	v_lshl_add_u64 v[28:29], s[8:9], 0, v[10:11]
	v_add_co_u32_e32 v32, vcc, 0x176000, v28
	v_lshl_add_u64 v[30:31], v[28:29], 0, s[0:1]
	s_nop 0
	v_addc_co_u32_e32 v33, vcc, 0, v29, vcc
	v_add_co_u32_e32 v44, vcc, 0x177000, v28
	global_load_dwordx4 v[12:15], v[30:31], off offset:1024
	global_load_dwordx4 v[16:19], v[30:31], off offset:2048
	global_load_dwordx4 v[20:23], v[32:33], off
	global_load_dwordx4 v[24:27], v[30:31], off offset:3072
	v_addc_co_u32_e32 v45, vcc, 0, v29, vcc
	global_load_dwordx4 v[28:31], v[44:45], off
	global_load_dwordx4 v[32:35], v[44:45], off offset:1024
	global_load_dwordx4 v[36:39], v[44:45], off offset:2048
	global_load_dwordx4 v[40:43], v[44:45], off offset:3072
	s_waitcnt vmcnt(5)
	v_pk_mul_f32 v[22:23], v[22:23], s[2:3] op_sel_hi:[1,0]
	v_pk_mul_f32 v[14:15], v[14:15], s[2:3] op_sel_hi:[1,0]
	v_pk_mul_f32 v[12:13], v[12:13], s[2:3] op_sel_hi:[1,0]
	v_pk_mul_f32 v[20:21], v[20:21], s[2:3] op_sel_hi:[1,0]
	s_nop 0
	v_cvt_pk_bf16_f32 v44, v20, v21
	v_cvt_pk_bf16_f32 v22, v22, v23
	v_cvt_pk_bf16_f32 v23, v12, v13
	v_cvt_pk_bf16_f32 v45, v14, v15
	v_pk_mul_f32 v[12:13], v[18:19], s[2:3] op_sel_hi:[1,0]
	v_pk_mul_f32 v[14:15], v[16:17], s[2:3] op_sel_hi:[1,0]
	s_nop 0
	v_cvt_pk_bf16_f32 v46, v14, v15
	v_cvt_pk_bf16_f32 v47, v12, v13
	s_waitcnt vmcnt(4)
	v_pk_mul_f32 v[12:13], v[26:27], s[2:3] op_sel_hi:[1,0]
	v_pk_mul_f32 v[14:15], v[24:25], s[2:3] op_sel_hi:[1,0]
	s_nop 0
	v_cvt_pk_bf16_f32 v48, v14, v15
	v_cvt_pk_bf16_f32 v49, v12, v13
	s_waitcnt vmcnt(3)
	v_pk_mul_f32 v[12:13], v[30:31], s[2:3] op_sel_hi:[1,0]
	v_pk_mul_f32 v[14:15], v[28:29], s[2:3] op_sel_hi:[1,0]
	s_nop 0
	v_cvt_pk_bf16_f32 v52, v14, v15
	v_cvt_pk_bf16_f32 v53, v12, v13
	s_waitcnt vmcnt(2)
	v_pk_mul_f32 v[12:13], v[34:35], s[2:3] op_sel_hi:[1,0]
	v_pk_mul_f32 v[14:15], v[32:33], s[2:3] op_sel_hi:[1,0]
	s_nop 0
	v_cvt_pk_bf16_f32 v54, v14, v15
	v_cvt_pk_bf16_f32 v55, v12, v13
	s_waitcnt vmcnt(1)
	v_pk_mul_f32 v[12:13], v[38:39], s[2:3] op_sel_hi:[1,0]
	v_pk_mul_f32 v[14:15], v[36:37], s[2:3] op_sel_hi:[1,0]
	s_nop 0
	v_cvt_pk_bf16_f32 v60, v14, v15
	v_cvt_pk_bf16_f32 v61, v12, v13
	s_waitcnt vmcnt(0)
	v_pk_mul_f32 v[12:13], v[42:43], s[2:3] op_sel_hi:[1,0]
	v_pk_mul_f32 v[14:15], v[40:41], s[2:3] op_sel_hi:[1,0]
	s_nop 0
	v_cvt_pk_bf16_f32 v62, v14, v15
	v_cvt_pk_bf16_f32 v63, v12, v13
	s_ashr_i32 s7, s6, 31
	s_lshl_b64 s[8:9], s[6:7], 6
	v_lshl_add_u64 v[12:13], v[0:1], 0, s[8:9]
	global_load_dword v127, v[12:13], off nt
	s_or_b32 s8, s6, 1
	s_lshl_b64 s[10:11], s[6:7], 12
	s_ashr_i32 s9, s8, 31
	v_lshl_add_u64 v[16:17], v[2:3], 0, s[10:11]
	s_lshl_b64 s[8:9], s[8:9], 6
	global_load_dwordx2 v[58:59], v[16:17], off nt
	global_load_dwordx2 v[56:57], v[16:17], off offset:512 nt
	global_load_dwordx2 v[50:51], v[16:17], off offset:1024 nt
	global_load_dwordx2 v[40:41], v[16:17], off offset:1536 nt
	global_load_dwordx2 v[30:31], v[16:17], off offset:2048 nt
	global_load_dwordx2 v[20:21], v[16:17], off offset:2560 nt
	global_load_dwordx2 v[14:15], v[16:17], off offset:3072 nt
	global_load_dwordx2 v[12:13], v[16:17], off offset:3584 nt
	v_lshl_add_u64 v[16:17], v[0:1], 0, s[8:9]
	global_load_dword v9, v[16:17], off nt
	v_lshlrev_b32_e32 v18, 16, v22
	v_and_b32_e32 v19, 0xffff0000, v22
	v_lshlrev_b32_e32 v22, 16, v23
	v_and_b32_e32 v23, 0xffff0000, v23
	v_lshlrev_b32_e32 v24, 16, v45
	v_and_b32_e32 v25, 0xffff0000, v45
	v_lshlrev_b32_e32 v26, 16, v46
	v_and_b32_e32 v27, 0xffff0000, v46
	v_lshlrev_b32_e32 v28, 16, v47
	v_and_b32_e32 v29, 0xffff0000, v47
	v_lshlrev_b32_e32 v32, 16, v48
	v_and_b32_e32 v33, 0xffff0000, v48
	v_lshlrev_b32_e32 v34, 16, v49
	v_and_b32_e32 v35, 0xffff0000, v49
	v_lshlrev_b32_e32 v36, 16, v52
	v_and_b32_e32 v37, 0xffff0000, v52
	v_lshlrev_b32_e32 v38, 16, v53
	v_and_b32_e32 v39, 0xffff0000, v53
	v_lshlrev_b32_e32 v42, 16, v54
	v_and_b32_e32 v43, 0xffff0000, v54
	v_and_b32_e32 v45, 0xffff0000, v55
	v_lshlrev_b32_e32 v46, 16, v60
	v_and_b32_e32 v47, 0xffff0000, v60
	v_lshlrev_b32_e32 v48, 16, v61
	v_and_b32_e32 v49, 0xffff0000, v61
	v_lshlrev_b32_e32 v52, 16, v62
	v_and_b32_e32 v53, 0xffff0000, v62
	v_lshlrev_b32_e32 v54, 16, v63
	v_mov_b32_e32 v77, -1
	s_waitcnt vmcnt(9)
	v_cmp_lt_i32_e64 s[8:9], -1, v127
	s_and_b32 s7, s8, 0xffff
	s_add_i32 s8, s8, -1
	s_and_b32 s10, s8, s7
	s_add_i32 s13, s10, -1
	s_cmp_eq_u32 s7, 0
	s_cselect_b64 s[8:9], -1, 0
	s_ff1_i32_b32 s11, s7
	v_cndmask_b32_e64 v78, 1.0, 0, s[8:9]
	s_and_b64 s[8:9], s[8:9], exec
	s_cselect_b32 s7, 0, s11
	v_readlane_b32 s8, v127, s7
	s_cselect_b32 s8, 0, s8
	s_ashr_i32 s9, s8, 31
	s_lshl_b64 s[8:9], s[8:9], 11
	s_cmp_eq_u32 s10, 0
	v_lshl_add_u64 v[16:17], v[4:5], 0, s[8:9]
	s_cselect_b64 s[8:9], -1, 0
	s_ff1_i32_b32 s14, s10
	v_cndmask_b32_e64 v76, 1.0, 0, s[8:9]
	s_and_b64 s[8:9], s[8:9], exec
	s_cselect_b32 s7, s7, s14
	v_readlane_b32 s7, v127, s7
	s_cselect_b32 s8, 0, s7
	s_ashr_i32 s9, s8, 31
	s_lshl_b64 s[8:9], s[8:9], 11
	global_load_dword v79, v[16:17], off nt
	global_load_dword v112, v[16:17], off offset:256 nt
	global_load_dword v113, v[16:17], off offset:512 nt
	global_load_dword v114, v[16:17], off offset:768 nt
	global_load_dword v115, v[16:17], off offset:1024 nt
	global_load_dword v116, v[16:17], off offset:1280 nt
	global_load_dword v117, v[16:17], off offset:1536 nt
	global_load_dword v118, v[16:17], off offset:1792 nt
	v_lshl_add_u64 v[16:17], v[4:5], 0, s[8:9]
	global_load_dword v119, v[16:17], off nt
	global_load_dword v120, v[16:17], off offset:256 nt
	global_load_dword v121, v[16:17], off offset:512 nt
	global_load_dword v122, v[16:17], off offset:768 nt
	global_load_dword v123, v[16:17], off offset:1024 nt
	global_load_dword v124, v[16:17], off offset:1280 nt
	global_load_dword v125, v[16:17], off offset:1536 nt
	global_load_dword v126, v[16:17], off offset:1792 nt
	s_and_b32 s13, s13, s10
	v_lshlrev_b32_e32 v16, 16, v44
	v_and_b32_e32 v17, 0xffff0000, v44
	v_lshlrev_b32_e32 v44, 16, v55
	v_and_b32_e32 v55, 0xffff0000, v63
	s_mov_b32 s7, 0
	s_branch .LBB0_2032

; #define CMB_LOADH(HP, row_) do { _Pragma("unroll") for (int j = 0; j < 8; ++j) HP[j] = *(const u32x2*)(H + (size_t)(row_) * DM + 4 * lane + 256 * j); } while (0)
; template <bool LAST> DI void cmb_block(bf16_t* H, const bf16_t* Y, const int* inv, const float* g2, const float* gain1, const float* shift, const float* scale, bf16_t* A, float* out, int row0, int n, int lane) {
;     ...
;     for (int i = 0; i < n; ++i) {
;         const int row = row0 + i; const bool more = i + 1 < n;
;         if (more) CMB_LOADH(hn, row + 1);
;         if (i + 2 < n) iv2 = CMB_INV(row + 2);
.LBB0_2032:
	s_add_i32 s8, s7, s6
	s_cmp_lt_u32 s7, 7
	s_cselect_b64 s[10:11], -1, 0
	s_cmp_gt_u32 s7, 6
	s_cbranch_scc1 .LBB0_2034
	s_ashr_i32 s9, s8, 31
	s_lshl_b64 s[14:15], s[8:9], 12
	v_lshl_add_u64 v[60:61], v[2:3], 0, s[14:15]
	v_lshl_add_u64 v[80:81], v[60:61], 0, s[4:5]
	v_add_co_u32_e32 v82, vcc, 0x1000, v60
	s_nop 1
	v_addc_co_u32_e32 v83, vcc, 0, v61, vcc
	global_load_dwordx2 v[66:67], v[80:81], off offset:512 nt
	global_load_dwordx2 v[64:65], v[80:81], off offset:1024 nt
	global_load_dwordx2 v[62:63], v[80:81], off offset:1536 nt
	global_load_dwordx2 v[60:61], v[80:81], off offset:2048 nt
	global_load_dwordx2 v[74:75], v[82:83], off nt
	global_load_dwordx2 v[72:73], v[80:81], off offset:2560 nt
	global_load_dwordx2 v[70:71], v[80:81], off offset:3072 nt
	global_load_dwordx2 v[68:69], v[80:81], off offset:3584 nt
.LBB0_2034:
	s_cmp_gt_u32 s7, 5
	s_cbranch_scc1 .LBB0_2036
	s_ashr_i32 s9, s8, 31
	s_lshl_b64 s[14:15], s[8:9], 6
	v_lshl_add_u64 v[80:81], v[0:1], 0, s[14:15]
	global_load_dword v77, v[80:81], off offset:128 nt

; DI f32x4 unpk4_fp8(unsigned w) { const f32x2 lo = __builtin_amdgcn_cvt_pk_f32_fp8((int)w, false), hi = __builtin_amdgcn_cvt_pk_f32_fp8((int)w, true); return (f32x4){lo.x, lo.y, hi.x, hi.y}; }
; template <bool LAST> DI void cmb_block(bf16_t* H, const bf16_t* Y, const int* inv, const float* g2, const float* gain1, const float* shift, const float* scale, bf16_t* A, float* out, int row0, int n, int lane) {
;     ...
;         while (m) {
;             CMB_GATHER(iv0);
; #pragma unroll
;             for (int j = 0; j < 8; ++j) acc[j] += unpk4_fp8(q1[j]) * f1 + unpk4_fp8(q2[j]) * f2;
;         }
.LBB0_2037:
	s_add_i32 s14, s13, -1
	s_ff1_i32_b32 s9, s13
	s_and_b32 s13, s14, s13
	v_sub_co_u32_e64 v78, s[16:17], s13, 1
	v_readlane_b32 s14, v127, s9
	s_ff1_i32_b32 s15, s13
	s_and_b64 s[18:19], s[16:17], exec
	s_cselect_b32 s9, s9, s15
	s_ashr_i32 s15, s14, 31
	s_lshl_b64 s[14:15], s[14:15], 11
	v_readlane_b32 s9, v127, s9
	v_lshl_add_u64 v[120:121], v[4:5], 0, s[14:15]
	s_and_b64 s[14:15], s[16:17], exec
	s_cselect_b32 s14, 0, s9
	s_ashr_i32 s15, s14, 31
	s_lshl_b64 s[14:15], s[14:15], 11
	v_lshl_add_u64 v[128:129], v[4:5], 0, s[14:15]
	global_load_dword v79, v[120:121], off nt
	global_load_dword v112, v[120:121], off offset:256 nt
	global_load_dword v113, v[120:121], off offset:512 nt
	global_load_dword v114, v[120:121], off offset:768 nt
	global_load_dword v115, v[120:121], off offset:1024 nt
	global_load_dword v116, v[120:121], off offset:1280 nt
	global_load_dword v117, v[120:121], off offset:1536 nt
	global_load_dword v118, v[120:121], off offset:1792 nt
	global_load_dword v119, v[128:129], off nt
	s_nop 0
	global_load_dword v120, v[128:129], off offset:256 nt
	global_load_dword v121, v[128:129], off offset:512 nt
	global_load_dword v122, v[128:129], off offset:768 nt
	global_load_dword v123, v[128:129], off offset:1024 nt
	global_load_dword v124, v[128:129], off offset:1280 nt
	global_load_dword v125, v[128:129], off offset:1536 nt
	global_load_dword v126, v[128:129], off offset:1792 nt
	v_cndmask_b32_e64 v76, 1.0, 0, s[16:17]
	v_readfirstlane_b32 s9, v78
	s_and_b32 s13, s9, s13
	s_cmp_lg_u32 s13, 0
	s_waitcnt vmcnt(7)
	v_cvt_pk_f32_fp8_e32 v[160:161], v119
	v_cvt_pk_f32_fp8_e32 v[128:129], v79
	v_cvt_pk_f32_fp8_sdwa v[130:131], v79 src0_sel:WORD_1
	v_cvt_pk_f32_fp8_e32 v[132:133], v112
	v_cvt_pk_f32_fp8_sdwa v[134:135], v112 src0_sel:WORD_1
	v_cvt_pk_f32_fp8_e32 v[136:137], v113
	v_cvt_pk_f32_fp8_sdwa v[138:139], v113 src0_sel:WORD_1
	v_cvt_pk_f32_fp8_e32 v[140:141], v114
	v_cvt_pk_f32_fp8_sdwa v[142:143], v114 src0_sel:WORD_1
	v_cvt_pk_f32_fp8_e32 v[144:145], v115
	v_cvt_pk_f32_fp8_sdwa v[146:147], v115 src0_sel:WORD_1
	v_cvt_pk_f32_fp8_e32 v[148:149], v116
	v_cvt_pk_f32_fp8_sdwa v[150:151], v116 src0_sel:WORD_1
	v_cvt_pk_f32_fp8_e32 v[152:153], v117
	v_cvt_pk_f32_fp8_sdwa v[154:155], v117 src0_sel:WORD_1
	v_cvt_pk_f32_fp8_e32 v[156:157], v118
	v_cvt_pk_f32_fp8_sdwa v[158:159], v118 src0_sel:WORD_1
	v_cvt_pk_f32_fp8_sdwa v[162:163], v119 src0_sel:WORD_1
	s_waitcnt vmcnt(6)
	v_cvt_pk_f32_fp8_e32 v[164:165], v120
	v_cvt_pk_f32_fp8_sdwa v[166:167], v120 src0_sel:WORD_1
	s_waitcnt vmcnt(5)
	v_cvt_pk_f32_fp8_e32 v[168:169], v121
	v_cvt_pk_f32_fp8_sdwa v[170:171], v121 src0_sel:WORD_1
	s_waitcnt vmcnt(4)
	v_cvt_pk_f32_fp8_e32 v[172:173], v122
	v_cvt_pk_f32_fp8_sdwa v[174:175], v122 src0_sel:WORD_1
	s_waitcnt vmcnt(3)
	v_cvt_pk_f32_fp8_e32 v[176:177], v123
	v_cvt_pk_f32_fp8_sdwa v[178:179], v123 src0_sel:WORD_1
	s_waitcnt vmcnt(2)
	v_cvt_pk_f32_fp8_e32 v[180:181], v124
	v_cvt_pk_f32_fp8_sdwa v[182:183], v124 src0_sel:WORD_1
	s_waitcnt vmcnt(1)
	v_cvt_pk_f32_fp8_e32 v[184:185], v125
	v_cvt_pk_f32_fp8_sdwa v[186:187], v125 src0_sel:WORD_1
	s_waitcnt vmcnt(0)
	v_cvt_pk_f32_fp8_e32 v[188:189], v126
	v_cvt_pk_f32_fp8_sdwa v[190:191], v126 src0_sel:WORD_1
	v_pk_fma_f32 v[128:129], v[76:77], v[160:161], v[128:129] op_sel_hi:[0,1,1]
	v_pk_fma_f32 v[130:131], v[76:77], v[162:163], v[130:131] op_sel_hi:[0,1,1]
	v_pk_fma_f32 v[132:133], v[76:77], v[164:165], v[132:133] op_sel_hi:[0,1,1]
	v_pk_fma_f32 v[134:135], v[76:77], v[166:167], v[134:135] op_sel_hi:[0,1,1]
	v_pk_fma_f32 v[136:137], v[76:77], v[168:169], v[136:137] op_sel_hi:[0,1,1]
	v_pk_fma_f32 v[138:139], v[76:77], v[170:171], v[138:139] op_sel_hi:[0,1,1]
	v_pk_fma_f32 v[140:141], v[76:77], v[172:173], v[140:141] op_sel_hi:[0,1,1]
	v_pk_fma_f32 v[142:143], v[76:77], v[174:175], v[142:143] op_sel_hi:[0,1,1]
	v_pk_fma_f32 v[144:145], v[76:77], v[176:177], v[144:145] op_sel_hi:[0,1,1]
	v_pk_fma_f32 v[146:147], v[76:77], v[178:179], v[146:147] op_sel_hi:[0,1,1]
	v_pk_fma_f32 v[148:149], v[76:77], v[180:181], v[148:149] op_sel_hi:[0,1,1]
	v_pk_fma_f32 v[150:151], v[76:77], v[182:183], v[150:151] op_sel_hi:[0,1,1]
	v_pk_fma_f32 v[152:153], v[76:77], v[184:185], v[152:153] op_sel_hi:[0,1,1]
	v_pk_fma_f32 v[154:155], v[76:77], v[186:187], v[154:155] op_sel_hi:[0,1,1]
	v_pk_fma_f32 v[156:157], v[76:77], v[188:189], v[156:157] op_sel_hi:[0,1,1]
	v_pk_fma_f32 v[158:159], v[76:77], v[190:191], v[158:159] op_sel_hi:[0,1,1]
	v_pk_add_f32 v[110:111], v[110:111], v[130:131]
	v_pk_add_f32 v[108:109], v[108:109], v[128:129]
	v_pk_add_f32 v[106:107], v[106:107], v[134:135]
	v_pk_add_f32 v[104:105], v[104:105], v[132:133]
	v_pk_add_f32 v[102:103], v[102:103], v[138:139]
	v_pk_add_f32 v[100:101], v[100:101], v[136:137]
	v_pk_add_f32 v[98:99], v[98:99], v[142:143]
	v_pk_add_f32 v[96:97], v[96:97], v[140:141]
	v_pk_add_f32 v[94:95], v[94:95], v[146:147]
	v_pk_add_f32 v[92:93], v[92:93], v[144:145]
	v_pk_add_f32 v[90:91], v[90:91], v[150:151]
	v_pk_add_f32 v[88:89], v[88:89], v[148:149]
	v_pk_add_f32 v[86:87], v[86:87], v[154:155]
	v_pk_add_f32 v[82:83], v[82:83], v[152:153]
	v_pk_add_f32 v[80:81], v[80:81], v[158:159]
	v_pk_add_f32 v[84:85], v[84:85], v[156:157]
	s_cbranch_scc1 .LBB0_2037
	v_mov_b32_e32 v78, 1.0
; #define CMB_FENCE() do { asm volatile("" ::: "memory"); __builtin_amdgcn_sched_barrier(0); } while (0)
; template <bool LAST> DI void cmb_block(bf16_t* H, const bf16_t* Y, const int* inv, const float* g2, const float* gain1, const float* shift, const float* scale, bf16_t* A, float* out, int row0, int n, int lane) {
;     ...
;         if (more) { m = (unsigned)(__ballot(iv1 >= 0) & 0xFFFFull); CMB_GATHER(iv1); }
;         CMB_FENCE();
.LBB0_2039:
	s_andn2_b64 vcc, exec, s[10:11]
	s_mov_b32 s13, 0
	s_cbranch_vccnz .LBB0_2031
	v_cmp_lt_i32_e64 s[10:11], -1, v9
	s_and_b32 s9, s10, 0xffff
	s_add_i32 s10, s10, -1
	s_and_b32 s13, s10, s9
	s_add_i32 s16, s13, -1
	s_cmp_eq_u32 s9, 0
	s_cselect_b64 s[10:11], -1, 0
	s_ff1_i32_b32 s9, s9
	v_cndmask_b32_e64 v78, 1.0, 0, s[10:11]
	s_and_b64 s[10:11], s[10:11], exec
	s_cselect_b32 s9, 0, s9
	v_readlane_b32 s10, v9, s9
	s_cselect_b32 s10, 0, s10
	s_ashr_i32 s11, s10, 31
	s_lshl_b64 s[10:11], s[10:11], 11
	s_cmp_eq_u32 s13, 0
	s_cselect_b64 s[14:15], -1, 0
	s_ff1_i32_b32 s17, s13
	v_cndmask_b32_e64 v76, 1.0, 0, s[14:15]
	s_and_b64 s[14:15], s[14:15], exec
	s_cselect_b32 s9, s9, s17
	v_readlane_b32 s9, v9, s9
	v_lshl_add_u64 v[124:125], v[4:5], 0, s[10:11]
	s_cselect_b32 s10, 0, s9
	s_ashr_i32 s11, s10, 31
	s_lshl_b64 s[10:11], s[10:11], 11
	v_lshl_add_u64 v[126:127], v[4:5], 0, s[10:11]
	global_load_dword v79, v[124:125], off nt
	global_load_dword v112, v[124:125], off offset:256 nt
	global_load_dword v113, v[124:125], off offset:512 nt
	global_load_dword v114, v[124:125], off offset:768 nt
	global_load_dword v115, v[124:125], off offset:1024 nt
	global_load_dword v116, v[124:125], off offset:1280 nt
	global_load_dword v117, v[124:125], off offset:1536 nt
	global_load_dword v118, v[124:125], off offset:1792 nt
	global_load_dword v119, v[126:127], off nt
	global_load_dword v120, v[126:127], off offset:256 nt
	global_load_dword v121, v[126:127], off offset:512 nt
	global_load_dword v122, v[126:127], off offset:768 nt
	global_load_dword v123, v[126:127], off offset:1024 nt
	global_load_dword v124, v[126:127], off offset:1280 nt
	global_load_dword v125, v[126:127], off offset:1536 nt
	s_nop 0
	global_load_dword v126, v[126:127], off offset:1792 nt
	s_and_b32 s13, s16, s13
	s_branch .LBB0_2031
